# conv tile wait relaxation (stage waits vmcnt(32), tap-loop wait vmcnt(10)) plus MoE position flush with its eight atomics issued together
# speedup vs baseline: 1.0085x; 1.0015x over previous
.LBB0_521:
	s_mov_b64 s[4:5], s[0:1]
	s_load_dwordx4 s[8:11], s[4:5], 0x48
	v_readlane_b32 s4, v255, 15
	v_readlane_b32 s5, v255, 16
	s_mov_b32 s6, s4
	s_mul_i32 s4, s4, 0xf800
	s_waitcnt lgkmcnt(0)
	s_add_u32 s4, s8, s4
	s_mul_hi_u32 s5, s6, 0xf800
	v_mbcnt_lo_u32_b32 v0, -1, 0
	v_mbcnt_hi_u32_b32 v0, -1, v0
	s_addc_u32 s5, s9, s5
	v_add_u32_e32 v2, s67, v0
	s_movk_i32 s6, 0x1780
	v_ashrrev_i32_e32 v3, 31, v2
	v_lshl_add_u64 v[4:5], v[2:3], 2, s[4:5]
	v_add_co_u32_e32 v6, vcc, s74, v4
	s_movk_i32 s4, 0x2000
	s_nop 0
	v_addc_co_u32_e32 v7, vcc, 0, v5, vcc
	v_add_co_u32_e32 v8, vcc, s4, v4
	s_movk_i32 s4, 0x3000
	s_nop 0
	v_addc_co_u32_e32 v9, vcc, 0, v5, vcc
	global_load_dword v42, v[4:5], off
	global_load_dword v44, v[4:5], off offset:2048
	global_load_dword v46, v[8:9], off offset:-4096
	global_load_dword v48, v[6:7], off offset:2048
	global_load_dword v50, v[8:9], off
	global_load_dword v52, v[8:9], off offset:2048
	v_add_co_u32_e32 v6, vcc, s4, v4
	s_movk_i32 s4, 0x4000
	s_nop 0
	v_addc_co_u32_e32 v7, vcc, 0, v5, vcc
	v_add_co_u32_e32 v8, vcc, s4, v4
	s_movk_i32 s4, 0x5000
	s_nop 0
	v_addc_co_u32_e32 v9, vcc, 0, v5, vcc
	global_load_dword v54, v[8:9], off offset:-4096
	global_load_dword v56, v[6:7], off offset:2048
	global_load_dword v58, v[8:9], off
	global_load_dword v60, v[8:9], off offset:2048
	v_add_co_u32_e32 v6, vcc, s4, v4
	s_movk_i32 s4, 0x6000
	s_nop 0
	v_addc_co_u32_e32 v7, vcc, 0, v5, vcc
	v_add_co_u32_e32 v8, vcc, s4, v4
	s_movk_i32 s4, 0x7000
	s_nop 0
	v_addc_co_u32_e32 v9, vcc, 0, v5, vcc
	global_load_dword v62, v[8:9], off offset:-4096
	global_load_dword v64, v[6:7], off offset:2048
	global_load_dword v114, v[8:9], off
	global_load_dword v116, v[8:9], off offset:2048
	v_add_co_u32_e32 v6, vcc, s4, v4
	s_mov_b32 s4, 0x8000
	s_nop 0
	v_addc_co_u32_e32 v7, vcc, 0, v5, vcc
	v_add_co_u32_e32 v8, vcc, s4, v4
	s_mov_b32 s4, 0x9000
	s_nop 0
	v_addc_co_u32_e32 v9, vcc, 0, v5, vcc
	global_load_dword v118, v[8:9], off offset:-4096
	global_load_dword v120, v[6:7], off offset:2048
	global_load_dword v122, v[8:9], off
	global_load_dword v124, v[8:9], off offset:2048
	v_add_co_u32_e32 v6, vcc, s4, v4
	s_mov_b32 s4, 0xa000
	s_nop 0
	v_addc_co_u32_e32 v7, vcc, 0, v5, vcc
	v_add_co_u32_e32 v8, vcc, s4, v4
	s_mov_b32 s4, 0xb000
	s_nop 0
	v_addc_co_u32_e32 v9, vcc, 0, v5, vcc
	global_load_dword v126, v[8:9], off offset:-4096
	global_load_dword v128, v[6:7], off offset:2048
	global_load_dword v130, v[8:9], off
	global_load_dword v132, v[8:9], off offset:2048
	v_add_co_u32_e32 v6, vcc, s4, v4
	s_mov_b32 s4, 0xc000
	s_nop 0
	v_addc_co_u32_e32 v7, vcc, 0, v5, vcc
	v_add_co_u32_e32 v8, vcc, s4, v4
	s_mov_b32 s4, 0xd000
	s_nop 0
	v_addc_co_u32_e32 v9, vcc, 0, v5, vcc
	global_load_dword v134, v[8:9], off offset:-4096
	global_load_dword v136, v[6:7], off offset:2048
	global_load_dword v138, v[8:9], off
	global_load_dword v140, v[8:9], off offset:2048
	v_add_co_u32_e32 v6, vcc, s4, v4
	s_mov_b32 s4, 0xe000
	s_nop 0
	v_addc_co_u32_e32 v7, vcc, 0, v5, vcc
	v_add_co_u32_e32 v8, vcc, s4, v4
	s_mov_b32 s4, 0xf000
	s_nop 0
	v_addc_co_u32_e32 v9, vcc, 0, v5, vcc
	v_add_u32_e32 v2, s52, v2
	global_load_dword v142, v[8:9], off offset:-4096
	global_load_dword v144, v[6:7], off offset:2048
	global_load_dword v146, v[8:9], off
	global_load_dword v148, v[8:9], off offset:2048
	v_add_co_u32_e32 v4, vcc, s4, v4
	v_ashrrev_i32_e32 v3, 31, v2
	s_nop 0
	v_addc_co_u32_e32 v5, vcc, 0, v5, vcc
	v_lshl_add_u64 v[2:3], v[2:3], 2, s[10:11]
	global_load_dword v150, v[4:5], off
	global_load_dword v152, v[2:3], off
	s_bfe_i32 s5, s34, 0x10019
	s_lshl_b32 s4, s34, 6
	s_lshr_b32 s5, s5, 21
	v_mbcnt_lo_u32_b32 v0, -1, 0
	v_mbcnt_hi_u32_b32 v0, -1, v0
	s_add_i32 s5, s4, s5
	v_add_u32_e32 v2, s67, v0
	s_and_b32 s5, s5, 0xfffff800
	v_lshlrev_b32_e32 v0, 4, v2
	s_sub_i32 s4, s4, s5
	v_and_b32_e32 v0, 0x3f0, v0
	s_sub_i32 s5, 29, s4
	v_add_u32_e32 v0, 0, v0
	v_cmp_gt_i32_e32 vcc, s6, v2
	s_and_saveexec_b64 s[6:7], vcc
	s_cbranch_execz .LBB0_523
	v_ashrrev_i32_e32 v3, 6, v2
	v_cmp_lt_i32_e32 vcc, s5, v3
	v_mad_u64_u32 v[8:9], s[8:9], v3, s44, v[0:1]
	s_waitcnt vmcnt(32)
	v_cndmask_b32_e32 v4, 0, v66, vcc
	v_cndmask_b32_e32 v5, 0, v67, vcc
	v_cndmask_b32_e32 v6, 0, v68, vcc
	v_cndmask_b32_e32 v7, 0, v69, vcc
	ds_write_b128 v8, v[4:7]
.LBB0_523:
	s_or_b64 exec, exec, s[6:7]
	s_movk_i32 s6, 0x1580
	v_cmp_gt_i32_e32 vcc, s6, v2
	s_and_saveexec_b64 s[6:7], vcc
	s_cbranch_execz .LBB0_525
	v_add_u32_e32 v3, 0x200, v2
	v_ashrrev_i32_e32 v3, 6, v3
	v_cmp_lt_i32_e32 vcc, s5, v3
	v_mad_u64_u32 v[8:9], s[8:9], v3, s44, v[0:1]
	s_waitcnt vmcnt(32)
	v_cndmask_b32_e32 v4, 0, v70, vcc
	v_cndmask_b32_e32 v5, 0, v71, vcc
	v_cndmask_b32_e32 v6, 0, v72, vcc
	v_cndmask_b32_e32 v7, 0, v73, vcc
	ds_write_b128 v8, v[4:7]
.LBB0_525:
	s_or_b64 exec, exec, s[6:7]
	s_movk_i32 s6, 0x1380
	v_cmp_gt_i32_e32 vcc, s6, v2
	s_and_saveexec_b64 s[6:7], vcc
	s_cbranch_execz .LBB0_527
	v_add_u32_e32 v3, 0x400, v2
	v_ashrrev_i32_e32 v3, 6, v3
	v_cmp_lt_i32_e32 vcc, s5, v3
	v_mad_u64_u32 v[8:9], s[8:9], v3, s44, v[0:1]
	s_waitcnt vmcnt(32)
	v_cndmask_b32_e32 v4, 0, v74, vcc
	v_cndmask_b32_e32 v5, 0, v75, vcc
	v_cndmask_b32_e32 v6, 0, v76, vcc
	v_cndmask_b32_e32 v7, 0, v77, vcc
	ds_write_b128 v8, v[4:7]
.LBB0_527:
	s_or_b64 exec, exec, s[6:7]
	s_movk_i32 s6, 0x1180
	v_cmp_gt_i32_e32 vcc, s6, v2
	s_and_saveexec_b64 s[6:7], vcc
	s_cbranch_execz .LBB0_529
	v_add_u32_e32 v3, 0x600, v2
	v_ashrrev_i32_e32 v3, 6, v3
	v_cmp_lt_i32_e32 vcc, s5, v3
	v_mad_u64_u32 v[8:9], s[8:9], v3, s44, v[0:1]
	s_waitcnt vmcnt(32)
	v_cndmask_b32_e32 v4, 0, v78, vcc
	v_cndmask_b32_e32 v5, 0, v79, vcc
	v_cndmask_b32_e32 v6, 0, v80, vcc
	v_cndmask_b32_e32 v7, 0, v81, vcc
	ds_write_b128 v8, v[4:7]
.LBB0_529:
	s_or_b64 exec, exec, s[6:7]
	s_movk_i32 s6, 0xf80
	v_cmp_gt_i32_e32 vcc, s6, v2
	s_and_saveexec_b64 s[6:7], vcc
	s_cbranch_execz .LBB0_531
	v_add_u32_e32 v3, 0x800, v2
	v_ashrrev_i32_e32 v3, 6, v3
	v_cmp_lt_i32_e32 vcc, s5, v3
	v_mad_u64_u32 v[8:9], s[8:9], v3, s44, v[0:1]
	s_waitcnt vmcnt(32)
	v_cndmask_b32_e32 v4, 0, v82, vcc
	v_cndmask_b32_e32 v5, 0, v83, vcc
	v_cndmask_b32_e32 v6, 0, v84, vcc
	v_cndmask_b32_e32 v7, 0, v85, vcc
	ds_write_b128 v8, v[4:7]
.LBB0_531:
	s_or_b64 exec, exec, s[6:7]
	s_movk_i32 s6, 0xd80
	v_cmp_gt_i32_e32 vcc, s6, v2
	s_and_saveexec_b64 s[6:7], vcc
	s_cbranch_execz .LBB0_533
	v_add_u32_e32 v3, 0xa00, v2
	v_ashrrev_i32_e32 v3, 6, v3
	v_cmp_lt_i32_e32 vcc, s5, v3
	v_mad_u64_u32 v[8:9], s[8:9], v3, s44, v[0:1]
	s_waitcnt vmcnt(32)
	v_cndmask_b32_e32 v4, 0, v86, vcc
	v_cndmask_b32_e32 v5, 0, v87, vcc
	v_cndmask_b32_e32 v6, 0, v88, vcc
	v_cndmask_b32_e32 v7, 0, v89, vcc
	ds_write_b128 v8, v[4:7]
.LBB0_533:
	s_or_b64 exec, exec, s[6:7]
	s_movk_i32 s6, 0xb80
	v_cmp_gt_i32_e32 vcc, s6, v2
	s_and_saveexec_b64 s[6:7], vcc
	s_cbranch_execz .LBB0_535
	v_add_u32_e32 v3, 0xc00, v2
	v_ashrrev_i32_e32 v3, 6, v3
	v_cmp_lt_i32_e32 vcc, s5, v3
	v_mad_u64_u32 v[8:9], s[8:9], v3, s44, v[0:1]
	s_waitcnt vmcnt(32)
	v_cndmask_b32_e32 v4, 0, v90, vcc
	v_cndmask_b32_e32 v5, 0, v91, vcc
	v_cndmask_b32_e32 v6, 0, v92, vcc
	v_cndmask_b32_e32 v7, 0, v93, vcc
	ds_write_b128 v8, v[4:7]
.LBB0_535:
	s_or_b64 exec, exec, s[6:7]
	s_movk_i32 s6, 0x980
	v_cmp_gt_i32_e32 vcc, s6, v2
	s_and_saveexec_b64 s[6:7], vcc
	s_cbranch_execz .LBB0_537
	v_add_u32_e32 v3, 0xe00, v2
	v_ashrrev_i32_e32 v3, 6, v3
	v_cmp_lt_i32_e32 vcc, s5, v3
	v_mad_u64_u32 v[8:9], s[8:9], v3, s44, v[0:1]
	s_waitcnt vmcnt(32)
	v_cndmask_b32_e32 v4, 0, v94, vcc
	v_cndmask_b32_e32 v5, 0, v95, vcc
	v_cndmask_b32_e32 v6, 0, v96, vcc
	v_cndmask_b32_e32 v7, 0, v97, vcc
	ds_write_b128 v8, v[4:7]
.LBB0_537:
	s_or_b64 exec, exec, s[6:7]
	s_movk_i32 s6, 0x780
	v_cmp_gt_i32_e32 vcc, s6, v2
	s_and_saveexec_b64 s[6:7], vcc
	s_cbranch_execz .LBB0_539
	v_add_u32_e32 v3, 0x1000, v2
	v_ashrrev_i32_e32 v3, 6, v3
	v_cmp_lt_i32_e32 vcc, s5, v3
	v_mad_u64_u32 v[8:9], s[8:9], v3, s44, v[0:1]
	s_waitcnt vmcnt(32)
	v_cndmask_b32_e32 v4, 0, v98, vcc
	v_cndmask_b32_e32 v5, 0, v99, vcc
	v_cndmask_b32_e32 v6, 0, v100, vcc
	v_cndmask_b32_e32 v7, 0, v101, vcc
	ds_write_b128 v8, v[4:7]
.LBB0_539:
	s_or_b64 exec, exec, s[6:7]
	s_movk_i32 s6, 0x580
	v_cmp_gt_i32_e32 vcc, s6, v2
	s_and_saveexec_b64 s[6:7], vcc
	s_cbranch_execz .LBB0_541
	v_add_u32_e32 v3, 0x1200, v2
	v_ashrrev_i32_e32 v3, 6, v3
	v_cmp_lt_i32_e32 vcc, s5, v3
	v_mad_u64_u32 v[8:9], s[8:9], v3, s44, v[0:1]
	s_waitcnt vmcnt(32)
	v_cndmask_b32_e32 v4, 0, v102, vcc
	v_cndmask_b32_e32 v5, 0, v103, vcc
	v_cndmask_b32_e32 v6, 0, v104, vcc
	v_cndmask_b32_e32 v7, 0, v105, vcc
	ds_write_b128 v8, v[4:7]
.LBB0_541:
	s_or_b64 exec, exec, s[6:7]
	s_movk_i32 s6, 0x380
	v_cmp_gt_i32_e32 vcc, s6, v2
	s_and_saveexec_b64 s[6:7], vcc
	s_cbranch_execz .LBB0_543
	v_add_u32_e32 v3, 0x1400, v2
	v_ashrrev_i32_e32 v3, 6, v3
	v_cmp_lt_i32_e32 vcc, s5, v3
	v_mad_u64_u32 v[8:9], s[8:9], v3, s44, v[0:1]
	s_waitcnt vmcnt(32)
	v_cndmask_b32_e32 v4, 0, v106, vcc
	v_cndmask_b32_e32 v5, 0, v107, vcc
	v_cndmask_b32_e32 v6, 0, v108, vcc
	v_cndmask_b32_e32 v7, 0, v109, vcc
	ds_write_b128 v8, v[4:7]
.LBB0_543:
	s_or_b64 exec, exec, s[6:7]
	s_movk_i32 s6, 0x180
	v_cmp_gt_i32_e32 vcc, s6, v2
	s_and_saveexec_b64 s[6:7], vcc
	s_cbranch_execz .LBB0_545
	v_add_u32_e32 v2, 0x1600, v2
	v_ashrrev_i32_e32 v6, 6, v2
	v_cmp_lt_i32_e32 vcc, s5, v6
	v_mad_u64_u32 v[6:7], s[8:9], v6, s44, v[0:1]
	s_waitcnt vmcnt(32)
	v_cndmask_b32_e32 v2, 0, v110, vcc
	v_cndmask_b32_e32 v3, 0, v111, vcc
	v_cndmask_b32_e32 v4, 0, v112, vcc
	v_cndmask_b32_e32 v5, 0, v113, vcc
	ds_write_b128 v6, v[2:5]
.LBB0_545:
	s_or_b64 exec, exec, s[6:7]
	s_mov_b64 s[6:7], s[0:1]
	s_waitcnt lgkmcnt(0)
	s_barrier
	s_load_dwordx2 s[6:7], s[6:7], 0xd0
	v_mbcnt_lo_u32_b32 v0, -1, 0
	v_mbcnt_hi_u32_b32 v0, -1, v0
	s_movk_i32 s5, 0x13c0
	v_add_u32_e32 v0, s67, v0
	s_waitcnt lgkmcnt(0)
	s_add_u32 s26, s6, 0x11c00000
	s_addc_u32 s27, s7, 0
	s_ashr_i32 s35, s34, 31
	s_lshl_b64 s[36:37], s[34:35], 6
	s_sub_i32 s4, 14, s4
	v_lshlrev_b32_e32 v2, 3, v0
	v_add_u32_e32 v4, 0x200, v0
	s_add_u32 s28, s36, -15
	v_and_b32_e32 v14, 0x1f8, v2
	v_ashrrev_i32_e32 v2, 6, v0
	v_ashrrev_i32_e32 v4, 6, v4
	s_addc_u32 s29, s37, -1
	v_cmp_gt_i32_e32 vcc, s5, v0
	v_cmp_lt_i32_e64 s[6:7], s4, v2
	v_ashrrev_i32_e32 v3, 31, v2
	v_ashrrev_i32_e32 v5, 31, v4
	v_lshl_add_u64 v[2:3], s[28:29], 0, v[2:3]
	s_and_b64 s[24:25], vcc, s[6:7]
	s_movk_i32 s5, 0x11c0
	v_cmp_lt_i32_e64 s[6:7], s4, v4
	v_lshl_add_u64 v[4:5], s[28:29], 0, v[4:5]
	v_lshlrev_b64 v[2:3], 9, v[2:3]
	v_cmp_gt_i32_e32 vcc, s5, v0
	v_lshlrev_b64 v[4:5], 9, v[4:5]
	v_or_b32_e32 v2, v2, v14
	v_or_b32_e32 v4, v4, v14
	s_and_b64 s[22:23], vcc, s[6:7]
	v_cndmask_b32_e64 v3, 0, v3, s[24:25]
	v_cndmask_b32_e64 v2, 0, v2, s[24:25]
	v_cndmask_b32_e64 v5, 0, v5, s[22:23]
	v_cndmask_b32_e64 v4, 0, v4, s[22:23]
	v_lshl_add_u64 v[2:3], v[2:3], 1, s[26:27]
	v_lshl_add_u64 v[4:5], v[4:5], 1, s[26:27]
	global_load_dwordx4 v[38:41], v[2:3], off
	global_load_dwordx4 v[26:29], v[4:5], off
	v_add_u32_e32 v2, 0x400, v0
	v_add_u32_e32 v4, 0x600, v0
	v_ashrrev_i32_e32 v2, 6, v2
	s_movk_i32 s5, 0xfc0
	v_ashrrev_i32_e32 v4, 6, v4
	v_cmp_gt_i32_e32 vcc, s5, v0
	v_cmp_lt_i32_e64 s[6:7], s4, v2
	v_ashrrev_i32_e32 v3, 31, v2
	v_ashrrev_i32_e32 v5, 31, v4
	v_lshl_add_u64 v[2:3], s[28:29], 0, v[2:3]
	s_and_b64 s[20:21], vcc, s[6:7]
	s_movk_i32 s5, 0xdc0
	v_cmp_lt_i32_e64 s[6:7], s4, v4
	v_lshl_add_u64 v[4:5], s[28:29], 0, v[4:5]
	v_lshlrev_b64 v[2:3], 9, v[2:3]
	v_cmp_gt_i32_e32 vcc, s5, v0
	v_lshlrev_b64 v[4:5], 9, v[4:5]
	v_or_b32_e32 v2, v2, v14
	v_or_b32_e32 v4, v4, v14
	s_and_b64 s[18:19], vcc, s[6:7]
	v_cndmask_b32_e64 v3, 0, v3, s[20:21]
	v_cndmask_b32_e64 v2, 0, v2, s[20:21]
	v_cndmask_b32_e64 v5, 0, v5, s[18:19]
	v_cndmask_b32_e64 v4, 0, v4, s[18:19]
	v_lshl_add_u64 v[2:3], v[2:3], 1, s[26:27]
	v_lshl_add_u64 v[4:5], v[4:5], 1, s[26:27]
	global_load_dwordx4 v[34:37], v[2:3], off
	global_load_dwordx4 v[18:21], v[4:5], off
	v_add_u32_e32 v2, 0x800, v0
	v_add_u32_e32 v4, 0xa00, v0
	v_ashrrev_i32_e32 v2, 6, v2
	s_movk_i32 s5, 0xbc0
	v_ashrrev_i32_e32 v4, 6, v4
	v_cmp_gt_i32_e32 vcc, s5, v0
	v_cmp_lt_i32_e64 s[6:7], s4, v2
	v_ashrrev_i32_e32 v3, 31, v2
	v_ashrrev_i32_e32 v5, 31, v4
	v_lshl_add_u64 v[2:3], s[28:29], 0, v[2:3]
	s_and_b64 s[16:17], vcc, s[6:7]
	s_movk_i32 s5, 0x9c0
	v_cmp_lt_i32_e64 s[6:7], s4, v4
	v_lshl_add_u64 v[4:5], s[28:29], 0, v[4:5]
	v_lshlrev_b64 v[2:3], 9, v[2:3]
	v_cmp_gt_i32_e32 vcc, s5, v0
	v_lshlrev_b64 v[4:5], 9, v[4:5]
	v_or_b32_e32 v2, v2, v14
	v_or_b32_e32 v4, v4, v14
	s_and_b64 s[14:15], vcc, s[6:7]
	v_cndmask_b32_e64 v3, 0, v3, s[16:17]
	v_cndmask_b32_e64 v2, 0, v2, s[16:17]
	v_cndmask_b32_e64 v5, 0, v5, s[14:15]
	v_cndmask_b32_e64 v4, 0, v4, s[14:15]
	v_lshl_add_u64 v[2:3], v[2:3], 1, s[26:27]
	v_lshl_add_u64 v[4:5], v[4:5], 1, s[26:27]
	global_load_dwordx4 v[30:33], v[2:3], off
	global_load_dwordx4 v[10:13], v[4:5], off
	v_add_u32_e32 v2, 0xc00, v0
	v_add_u32_e32 v4, 0xe00, v0
	v_ashrrev_i32_e32 v2, 6, v2
	s_movk_i32 s5, 0x7c0
	v_ashrrev_i32_e32 v4, 6, v4
	v_cmp_gt_i32_e32 vcc, s5, v0
	v_cmp_lt_i32_e64 s[6:7], s4, v2
	v_ashrrev_i32_e32 v3, 31, v2
	v_ashrrev_i32_e32 v5, 31, v4
	v_lshl_add_u64 v[2:3], s[28:29], 0, v[2:3]
	s_and_b64 s[12:13], vcc, s[6:7]
	s_movk_i32 s5, 0x5c0
	v_cmp_lt_i32_e64 s[6:7], s4, v4
	v_lshl_add_u64 v[4:5], s[28:29], 0, v[4:5]
	v_lshlrev_b64 v[2:3], 9, v[2:3]
	v_cmp_gt_i32_e32 vcc, s5, v0
	v_lshlrev_b64 v[4:5], 9, v[4:5]
	v_or_b32_e32 v2, v2, v14
	v_or_b32_e32 v4, v4, v14
	s_and_b64 s[10:11], vcc, s[6:7]
	v_cndmask_b32_e64 v3, 0, v3, s[12:13]
	v_cndmask_b32_e64 v2, 0, v2, s[12:13]
	v_cndmask_b32_e64 v5, 0, v5, s[10:11]
	v_cndmask_b32_e64 v4, 0, v4, s[10:11]
	v_lshl_add_u64 v[2:3], v[2:3], 1, s[26:27]
	v_lshl_add_u64 v[4:5], v[4:5], 1, s[26:27]
	global_load_dwordx4 v[22:25], v[2:3], off
	global_load_dwordx4 v[6:9], v[4:5], off
	v_add_u32_e32 v2, 0x1000, v0
	v_add_u32_e32 v4, 0x1200, v0
	v_ashrrev_i32_e32 v2, 6, v2
	s_movk_i32 s5, 0x3c0
	v_ashrrev_i32_e32 v4, 6, v4
	v_cmp_gt_i32_e32 vcc, s5, v0
	v_cmp_lt_i32_e64 s[6:7], s4, v2
	v_ashrrev_i32_e32 v3, 31, v2
	v_ashrrev_i32_e32 v5, 31, v4
	v_lshl_add_u64 v[2:3], s[28:29], 0, v[2:3]
	s_and_b64 s[8:9], vcc, s[6:7]
	s_movk_i32 s5, 0x1c0
	v_cmp_lt_i32_e64 s[6:7], s4, v4
	v_lshl_add_u64 v[4:5], s[28:29], 0, v[4:5]
	v_lshlrev_b64 v[2:3], 9, v[2:3]
	v_cmp_gt_i32_e32 vcc, s5, v0
	v_lshlrev_b64 v[4:5], 9, v[4:5]
	v_or_b32_e32 v2, v2, v14
	v_or_b32_e32 v0, v4, v14
	s_and_b64 s[6:7], vcc, s[6:7]
	v_cndmask_b32_e64 v3, 0, v3, s[8:9]
	v_cndmask_b32_e64 v2, 0, v2, s[8:9]
	v_cndmask_b32_e64 v5, 0, v5, s[6:7]
	v_cndmask_b32_e64 v4, 0, v0, s[6:7]
	v_lshl_add_u64 v[2:3], v[2:3], 1, s[26:27]
	v_lshl_add_u64 v[4:5], v[4:5], 1, s[26:27]
	global_load_dwordx4 v[14:17], v[2:3], off
	s_nop 0
	global_load_dwordx4 v[2:5], v[4:5], off
	s_mov_b64 s[4:5], s[0:1]
	s_load_dwordx2 s[28:29], s[4:5], 0xd0
	s_load_dwordx2 s[26:27], s[4:5], 0x58
	v_mbcnt_lo_u32_b32 v0, -1, 0
	v_mbcnt_hi_u32_b32 v0, -1, v0
	s_mov_b32 s30, 0
	v_add_u32_e32 v0, s67, v0
	s_mov_b32 s31, 1
	s_waitcnt vmcnt(10)
	v_mov_b32_e32 v43, v42
	v_lshl_add_u32 v222, v0, 1, 0
	v_mov_b32_e32 v153, v152
	v_mov_b32_e32 v45, v44
	v_mov_b32_e32 v47, v46
	v_mov_b32_e32 v49, v48
	v_mov_b32_e32 v51, v50
	v_mov_b32_e32 v53, v52
	v_mov_b32_e32 v55, v54
	v_mov_b32_e32 v57, v56
	v_mov_b32_e32 v59, v58
	v_mov_b32_e32 v61, v60
	v_mov_b32_e32 v63, v62
	v_mov_b32_e32 v65, v64
	v_mov_b32_e32 v115, v114
	v_mov_b32_e32 v117, v116
	v_mov_b32_e32 v119, v118
	v_mov_b32_e32 v121, v120
	v_mov_b32_e32 v123, v122
	v_mov_b32_e32 v125, v124
	v_mov_b32_e32 v127, v126
	v_mov_b32_e32 v129, v128
	v_mov_b32_e32 v131, v130
	v_mov_b32_e32 v133, v132
	v_mov_b32_e32 v135, v134
	v_mov_b32_e32 v137, v136
	v_mov_b32_e32 v139, v138
	v_mov_b32_e32 v141, v140
	v_mov_b32_e32 v143, v142
	v_mov_b32_e32 v145, v144
	v_mov_b32_e32 v147, v146
	v_mov_b32_e32 v149, v148
	v_mov_b32_e32 v151, v150
	s_mov_b32 s33, 8

.LBB0_959:
	s_or_b64 exec, exec, s[20:21]
	v_sub_f32_e32 v165, v168, v165
	v_mul_f32_e32 v165, 0x3fb8aa3b, v165
	v_exp_f32_e32 v165, v165
	s_lshl_b32 s4, s44, 1
	v_cmp_eq_u32_e32 vcc, s4, v182
	v_add_f32_e32 v165, 1.0, v165
	v_rcp_f32_e32 v165, v165
	s_and_saveexec_b64 s[18:19], vcc
	v_mov_b32_e32 v203, 0
	v_mov_b32_e32 v183, s40
	v_mov_b32_e32 v155, v165
	v_mov_b32_e32 v154, v164
	s_or_b64 exec, exec, s[18:19]
	s_or_b32 s4, s4, 1
	v_cmp_eq_u32_e32 vcc, s4, v182
	s_and_saveexec_b64 s[18:19], vcc
	v_sub_f32_e32 v155, 1.0, v165
	v_mov_b32_e32 v203, 1
	v_mov_b32_e32 v183, s40
	v_mov_b32_e32 v154, v166
	s_or_b64 exec, exec, s[18:19]
	s_add_i32 s44, s44, 1
	s_cmp_lg_u32 s44, 32
	s_cselect_b64 s[4:5], -1, 0
	s_cmp_lt_i32 s33, 0x8000
	s_cselect_b64 s[18:19], -1, 0
	s_and_b64 s[4:5], s[4:5], s[18:19]
	s_and_b64 vcc, exec, s[4:5]
	s_cbranch_vccnz .LBB0_948
	v_mov_b32_e32 v164, 0
	v_cmp_eq_u32_e32 vcc, 0, v154
	s_cbranch_vccz .Lmfl_a0
	s_ff1_i32_b64 s4, vcc
	s_bcnt1_i32_b64 s5, vcc
	v_cmp_eq_u32_e64 s[18:19], s4, v182
	s_and_saveexec_b64 s[20:21], s[18:19]
	v_mov_b32_e32 v220, s5
	global_atomic_add v220, v1, v220, s[34:35] sc0
	s_mov_b64 exec, s[20:21]
.Lmfl_a0:
	v_cmp_eq_u32_e32 vcc, 1, v154
	s_cbranch_vccz .Lmfl_a1
	s_ff1_i32_b64 s4, vcc
	s_bcnt1_i32_b64 s5, vcc
	v_cmp_eq_u32_e64 s[18:19], s4, v182
	s_and_saveexec_b64 s[20:21], s[18:19]
	v_mov_b32_e32 v221, s5
	global_atomic_add v221, v1, v221, s[34:35] offset:256 sc0
	s_mov_b64 exec, s[20:21]
.Lmfl_a1:
	v_cmp_eq_u32_e32 vcc, 2, v154
	s_cbranch_vccz .Lmfl_a2
	s_ff1_i32_b64 s4, vcc
	s_bcnt1_i32_b64 s5, vcc
	v_cmp_eq_u32_e64 s[18:19], s4, v182
	s_and_saveexec_b64 s[20:21], s[18:19]
	v_mov_b32_e32 v222, s5
	global_atomic_add v222, v1, v222, s[34:35] offset:512 sc0
	s_mov_b64 exec, s[20:21]
.Lmfl_a2:
	v_cmp_eq_u32_e32 vcc, 3, v154
	s_cbranch_vccz .Lmfl_a3
	s_ff1_i32_b64 s4, vcc
	s_bcnt1_i32_b64 s5, vcc
	v_cmp_eq_u32_e64 s[18:19], s4, v182
	s_and_saveexec_b64 s[20:21], s[18:19]
	v_mov_b32_e32 v223, s5
	global_atomic_add v223, v1, v223, s[34:35] offset:768 sc0
	s_mov_b64 exec, s[20:21]
.Lmfl_a3:
	v_cmp_eq_u32_e32 vcc, 4, v154
	s_cbranch_vccz .Lmfl_a4
	s_ff1_i32_b64 s4, vcc
	s_bcnt1_i32_b64 s5, vcc
	v_cmp_eq_u32_e64 s[18:19], s4, v182
	s_and_saveexec_b64 s[20:21], s[18:19]
	v_mov_b32_e32 v224, s5
	global_atomic_add v224, v1, v224, s[34:35] offset:1024 sc0
	s_mov_b64 exec, s[20:21]
.Lmfl_a4:
	v_cmp_eq_u32_e32 vcc, 5, v154
	s_cbranch_vccz .Lmfl_a5
	s_ff1_i32_b64 s4, vcc
	s_bcnt1_i32_b64 s5, vcc
	v_cmp_eq_u32_e64 s[18:19], s4, v182
	s_and_saveexec_b64 s[20:21], s[18:19]
	v_mov_b32_e32 v225, s5
	global_atomic_add v225, v1, v225, s[34:35] offset:1280 sc0
	s_mov_b64 exec, s[20:21]
.Lmfl_a5:
	v_cmp_eq_u32_e32 vcc, 6, v154
	s_cbranch_vccz .Lmfl_a6
	s_ff1_i32_b64 s4, vcc
	s_bcnt1_i32_b64 s5, vcc
	v_cmp_eq_u32_e64 s[18:19], s4, v182
	s_and_saveexec_b64 s[20:21], s[18:19]
	v_mov_b32_e32 v226, s5
	global_atomic_add v226, v1, v226, s[34:35] offset:1536 sc0
	s_mov_b64 exec, s[20:21]
.Lmfl_a6:
	v_cmp_eq_u32_e32 vcc, 7, v154
	s_cbranch_vccz .Lmfl_a7
	s_ff1_i32_b64 s4, vcc
	s_bcnt1_i32_b64 s5, vcc
	v_cmp_eq_u32_e64 s[18:19], s4, v182
	s_and_saveexec_b64 s[20:21], s[18:19]
	v_mov_b32_e32 v227, s5
	global_atomic_add v227, v1, v227, s[34:35] offset:1792 sc0
	s_mov_b64 exec, s[20:21]
.Lmfl_a7:
	s_waitcnt vmcnt(0)
	v_cmp_eq_u32_e32 vcc, 0, v154
	s_cbranch_vccz .Lmfl_b0
	s_ff1_i32_b64 s4, vcc
	v_and_b32_e32 v167, vcc_lo, v148
	v_and_b32_e32 v166, vcc_hi, v149
	v_bcnt_u32_b32 v167, v167, 0
	v_bcnt_u32_b32 v166, v166, v167
	v_readlane_b32 s18, v220, s4
	s_nop 1
	v_add_u32_e32 v165, s18, v166
	v_cndmask_b32_e32 v164, v164, v165, vcc
.Lmfl_b0:
	v_cmp_eq_u32_e32 vcc, 1, v154
	s_cbranch_vccz .Lmfl_b1
	s_ff1_i32_b64 s4, vcc
	v_and_b32_e32 v167, vcc_lo, v148
	v_and_b32_e32 v166, vcc_hi, v149
	v_bcnt_u32_b32 v167, v167, 0
	v_bcnt_u32_b32 v166, v166, v167
	v_readlane_b32 s18, v221, s4
	s_nop 1
	v_add_u32_e32 v165, s18, v166
	v_cndmask_b32_e32 v164, v164, v165, vcc
.Lmfl_b1:
	v_cmp_eq_u32_e32 vcc, 2, v154
	s_cbranch_vccz .Lmfl_b2
	s_ff1_i32_b64 s4, vcc
	v_and_b32_e32 v167, vcc_lo, v148
	v_and_b32_e32 v166, vcc_hi, v149
	v_bcnt_u32_b32 v167, v167, 0
	v_bcnt_u32_b32 v166, v166, v167
	v_readlane_b32 s18, v222, s4
	s_nop 1
	v_add_u32_e32 v165, s18, v166
	v_cndmask_b32_e32 v164, v164, v165, vcc
.Lmfl_b2:
	v_cmp_eq_u32_e32 vcc, 3, v154
	s_cbranch_vccz .Lmfl_b3
	s_ff1_i32_b64 s4, vcc
	v_and_b32_e32 v167, vcc_lo, v148
	v_and_b32_e32 v166, vcc_hi, v149
	v_bcnt_u32_b32 v167, v167, 0
	v_bcnt_u32_b32 v166, v166, v167
	v_readlane_b32 s18, v223, s4
	s_nop 1
	v_add_u32_e32 v165, s18, v166
	v_cndmask_b32_e32 v164, v164, v165, vcc
.Lmfl_b3:
	v_cmp_eq_u32_e32 vcc, 4, v154
	s_cbranch_vccz .Lmfl_b4
	s_ff1_i32_b64 s4, vcc
	v_and_b32_e32 v167, vcc_lo, v148
	v_and_b32_e32 v166, vcc_hi, v149
	v_bcnt_u32_b32 v167, v167, 0
	v_bcnt_u32_b32 v166, v166, v167
	v_readlane_b32 s18, v224, s4
	s_nop 1
	v_add_u32_e32 v165, s18, v166
	v_cndmask_b32_e32 v164, v164, v165, vcc
.Lmfl_b4:
	v_cmp_eq_u32_e32 vcc, 5, v154
	s_cbranch_vccz .Lmfl_b5
	s_ff1_i32_b64 s4, vcc
	v_and_b32_e32 v167, vcc_lo, v148
	v_and_b32_e32 v166, vcc_hi, v149
	v_bcnt_u32_b32 v167, v167, 0
	v_bcnt_u32_b32 v166, v166, v167
	v_readlane_b32 s18, v225, s4
	s_nop 1
	v_add_u32_e32 v165, s18, v166
	v_cndmask_b32_e32 v164, v164, v165, vcc
.Lmfl_b5:
	v_cmp_eq_u32_e32 vcc, 6, v154
	s_cbranch_vccz .Lmfl_b6
	s_ff1_i32_b64 s4, vcc
	v_and_b32_e32 v167, vcc_lo, v148
	v_and_b32_e32 v166, vcc_hi, v149
	v_bcnt_u32_b32 v167, v167, 0
	v_bcnt_u32_b32 v166, v166, v167
	v_readlane_b32 s18, v226, s4
	s_nop 1
	v_add_u32_e32 v165, s18, v166
	v_cndmask_b32_e32 v164, v164, v165, vcc
.Lmfl_b6:
	v_cmp_eq_u32_e32 vcc, 7, v154
	s_cbranch_vccz .Lmfl_b7
	s_ff1_i32_b64 s4, vcc
	v_and_b32_e32 v167, vcc_lo, v148
	v_and_b32_e32 v166, vcc_hi, v149
	v_bcnt_u32_b32 v167, v167, 0
	v_bcnt_u32_b32 v166, v166, v167
	v_readlane_b32 s18, v227, s4
	s_nop 1
	v_add_u32_e32 v165, s18, v166
	v_cndmask_b32_e32 v164, v164, v165, vcc
.Lmfl_b7:
.LBB0_1012:
	v_cmp_lt_i32_e32 vcc, -1, v154
	s_and_saveexec_b64 s[18:19], vcc
	s_cbranch_execz .LBB0_947
	v_lshl_add_u32 v166, v183, 1, v203
	v_ashrrev_i32_e32 v167, 31, v166
	v_lshl_add_u64 v[166:167], v[166:167], 3, s[30:31]
	v_lshl_or_b32 v154, v154, 24, v164
	global_store_dwordx2 v[166:167], v[154:155], off
	s_branch .LBB0_947
